# v67 + P7 per-token sum-of-squares reduction: last in-row hop (xor 1) via DPP quad_perm instead of ds_bpermute (no LDS round trip left in P7 reductions)
# baseline (speedup 1.0000x reference)
; DI void p7_ln2(const Ctx& c) {
;     ...
;         float q2 = (lane < 32) ? ssq[(size_t)tok * 32 + lane] : 0.f;
; #pragma unroll
;         for (int o = 32; o >= 1; o >>= 1) q2 += __shfl_xor(q2, o);
;         if (lane == 0) rse[tok] = rsqrtf(q2 * (1.0f / D) + LN_EPS); }
.LBB0_979:
	s_or_b64 exec, exec, s[10:11]
	s_waitcnt vmcnt(0)
	v_mov_b32_e32 v1, v0
	s_nop 1
	v_permlane32_swap_b32 v0, v1
	v_add_f32_e32 v0, v0, v1
	v_mov_b32_e32 v1, v0
	s_nop 1
	v_permlane16_swap_b32 v0, v1
	v_add_f32_e32 v0, v0, v1
	s_nop 1
	v_add_f32_dpp v0, v0, v0 row_ror:8 row_mask:0xf bank_mask:0xf
	s_nop 1
	v_add_f32_dpp v0, v0, v0 row_ror:4 row_mask:0xf bank_mask:0xf
	s_nop 1
	v_add_f32_dpp v0, v0, v0 quad_perm:[2,3,0,1] row_mask:0xf bank_mask:0xf
	s_nop 1
	v_add_f32_dpp v0, v0, v0 quad_perm:[1,0,3,2] row_mask:0xf bank_mask:0xf
	s_and_saveexec_b64 s[22:23], s[6:7]
	s_cbranch_execz .LBB0_976
	v_fmamk_f32 v0, v0, 0x3a000000, v100
	v_mul_f32_e32 v1, 0x4b800000, v0
	v_cmp_gt_f32_e64 s[10:11], s27, v0
	s_add_u32 s36, s34, s30
	s_addc_u32 s37, s35, s31
	v_cndmask_b32_e64 v0, v0, v1, s[10:11]
	v_rsq_f32_e32 v0, v0
	s_nop 0
	v_mul_f32_e32 v1, 0x45800000, v0
	v_cndmask_b32_e64 v0, v0, v1, s[10:11]
	global_store_dword v58, v0, s[36:37]
	s_branch .LBB0_976
